# k_bsort buckets assigned to XCDs in runs of 16 as well
# speedup vs baseline: 1.0087x; 1.0018x over previous
_Z7k_bsortPK15HIP_vector_typeIfLj2EEPKiS4_PS_IfLj4EEPi:
	s_and_b32 s6, s2, 7
	s_lshl_b32 s6, s6, 4
	s_bfe_u32 s7, s2, 0x40003
	s_or_b32 s6, s6, s7
	s_and_b32 s7, s2, 0xffffff80
	s_or_b32 s6, s6, s7
	s_cmp_lt_u32 s2, 0x180
	s_cselect_b32 s2, s6, s2
	s_load_dwordx4 s[20:23], s[0:1], 0x0
	s_movk_i32 s3, 0x80
	v_cmp_gt_u32_e64 s[4:5], s3, v0
	v_lshlrev_b32_e32 v10, 2, v0
	s_and_saveexec_b64 s[6:7], s[4:5]
	v_mov_b32_e32 v1, 0
	ds_write_b32 v10, v1
	s_or_b64 exec, exec, s[6:7]
	s_ashr_i32 s3, s2, 31
	s_lshl_b64 s[6:7], s[2:3], 2
	s_waitcnt lgkmcnt(0)
	s_add_u32 s6, s22, s6
	s_addc_u32 s7, s23, s7
	s_load_dwordx2 s[14:15], s[6:7], 0x0
	s_load_dwordx2 s[28:29], s[0:1], 0x10
	s_mov_b64 s[8:9], -1
	s_waitcnt lgkmcnt(0)
	s_barrier
	s_sub_i32 s3, s15, s14
	s_cmpk_gt_i32 s3, 0xa00
	s_cselect_b64 s[6:7], -1, 0
	s_cmpk_lt_i32 s3, 0xa01
	v_add_u32_e32 v20, s14, v0
	s_cbranch_scc1 .LBB2_22
	s_mov_b32 s10, 0
	v_mov_b32_e32 v1, 1
	s_branch .LBB2_5
